# add batched GEMM1 prestep loads and batched P1 quantiser gain loads
# speedup vs baseline: 1.0125x; 1.0013x over previous
.LBB0_650:
	s_ashr_i32 s8, s50, 11
	s_ashr_i32 s9, s8, 31
	v_readlane_b32 s72, v251, 18
	s_lshl_b64 s[6:7], s[8:9], 24
	v_readlane_b32 s82, v251, 28
	v_readlane_b32 s83, v251, 29
	s_add_u32 s53, s82, s6
	s_addc_u32 s55, s83, s7
	s_and_b32 s6, s50, 0xfffff800
	s_ashr_i32 s7, s6, 31
	v_readlane_b32 s78, v251, 24
	s_lshl_b64 s[6:7], s[6:7], 2
	v_readlane_b32 s79, v251, 25
	s_add_u32 s10, s78, s6
	s_addc_u32 s11, s79, s7
	s_lshl_b32 s51, s50, 5
	s_and_b32 s51, s51, 0x7e0
	s_and_b32 s52, s50, 0x7c0
	s_lshl_b32 s54, s51, 2
	v_add_u32_e32 v6, s52, v24
	s_add_u32 s54, s53, s54
	s_addc_u32 s55, s55, 0
	v_ashrrev_i32_e32 v7, 31, v6
	v_lshl_add_u64 v[4:5], s[54:55], 0, v[2:3]
	v_lshlrev_b64 v[8:9], 13, v[6:7]
	v_lshl_add_u64 v[4:5], v[4:5], 0, v[8:9]
	s_movk_i32 s53, 0x4000
	v_add_co_u32_e32 v8, vcc, s53, v4
	v_lshl_add_u64 v[6:7], v[6:7], 2, s[10:11]
	s_nop 0
	v_addc_co_u32_e32 v9, vcc, 0, v5, vcc
	v_add_co_u32_e32 v10, vcc, s18, v4
	v_readlane_b32 s73, v251, 19
	s_nop 0
	v_addc_co_u32_e32 v11, vcc, 0, v5, vcc
	v_add_co_u32_e32 v12, vcc, s19, v4
	v_readlane_b32 s74, v251, 20
	s_nop 0
	v_addc_co_u32_e32 v13, vcc, 0, v5, vcc
	v_add_co_u32_e32 v14, vcc, s20, v4
	v_readlane_b32 s75, v251, 21
	s_nop 0
	v_addc_co_u32_e32 v15, vcc, 0, v5, vcc
	v_add_co_u32_e32 v16, vcc, s21, v4
	v_readlane_b32 s76, v251, 22
	s_nop 0
	v_addc_co_u32_e32 v17, vcc, 0, v5, vcc
	v_add_co_u32_e32 v18, vcc, s22, v4
	v_readlane_b32 s77, v251, 23
	s_nop 0
	v_addc_co_u32_e32 v19, vcc, 0, v5, vcc
	v_add_co_u32_e32 v22, vcc, s23, v4
	v_readlane_b32 s80, v251, 26
	s_nop 0
	v_addc_co_u32_e32 v23, vcc, 0, v5, vcc
	global_load_dword v56, v[4:5], off
	global_load_dword v57, v[8:9], off
	global_load_dword v20, v[10:11], off
	global_load_dword v21, v[12:13], off
	global_load_dword v54, v[14:15], off
	global_load_dword v55, v[16:17], off
	s_nop 0
	global_load_dword v18, v[18:19], off
	s_nop 0
	global_load_dword v19, v[22:23], off
	v_add_co_u32_e32 v8, vcc, s24, v4
	v_readlane_b32 s81, v251, 27
	s_nop 0
	v_addc_co_u32_e32 v9, vcc, 0, v5, vcc
	v_add_co_u32_e32 v10, vcc, s25, v4
	v_readlane_b32 s84, v251, 30
	s_nop 0
	v_addc_co_u32_e32 v11, vcc, 0, v5, vcc
	v_add_co_u32_e32 v12, vcc, s26, v4
	v_readlane_b32 s85, v251, 31
	s_nop 0
	v_addc_co_u32_e32 v13, vcc, 0, v5, vcc
	v_add_co_u32_e32 v14, vcc, s27, v4
	v_readlane_b32 s86, v251, 32
	s_nop 0
	v_addc_co_u32_e32 v15, vcc, 0, v5, vcc
	v_add_co_u32_e32 v22, vcc, s28, v4
	v_readlane_b32 s87, v251, 33
	s_nop 0
	v_addc_co_u32_e32 v23, vcc, 0, v5, vcc
	v_add_co_u32_e32 v42, vcc, s29, v4
	s_nop 1
	v_addc_co_u32_e32 v43, vcc, 0, v5, vcc
	v_add_co_u32_e32 v44, vcc, s30, v4
	s_nop 1
	v_addc_co_u32_e32 v45, vcc, 0, v5, vcc
	v_add_co_u32_e32 v46, vcc, s31, v4
	s_nop 1
	v_addc_co_u32_e32 v47, vcc, 0, v5, vcc
	global_load_dword v52, v[8:9], off
	global_load_dword v53, v[10:11], off
	global_load_dword v16, v[12:13], off
	global_load_dword v17, v[14:15], off
	global_load_dword v50, v[22:23], off
	global_load_dword v51, v[42:43], off
	s_nop 0
	global_load_dword v14, v[44:45], off
	global_load_dword v15, v[46:47], off
	v_add_co_u32_e32 v8, vcc, s34, v4
	s_nop 1
	v_addc_co_u32_e32 v9, vcc, 0, v5, vcc
	v_add_co_u32_e32 v10, vcc, s35, v4
	s_nop 1
	v_addc_co_u32_e32 v11, vcc, 0, v5, vcc
	v_add_co_u32_e32 v12, vcc, s36, v4
	s_nop 1
	v_addc_co_u32_e32 v13, vcc, 0, v5, vcc
	v_add_co_u32_e32 v22, vcc, s37, v4
	s_nop 1
	v_addc_co_u32_e32 v23, vcc, 0, v5, vcc
	v_add_co_u32_e32 v42, vcc, s38, v4
	s_nop 1
	v_addc_co_u32_e32 v43, vcc, 0, v5, vcc
	v_add_co_u32_e32 v46, vcc, s39, v4
	s_nop 1
	v_addc_co_u32_e32 v47, vcc, 0, v5, vcc
	v_add_co_u32_e32 v58, vcc, s40, v4
	s_nop 1
	v_addc_co_u32_e32 v59, vcc, 0, v5, vcc
	v_add_co_u32_e32 v60, vcc, s41, v4
	s_nop 1
	v_addc_co_u32_e32 v61, vcc, 0, v5, vcc
	global_load_dword v48, v[8:9], off
	global_load_dword v49, v[10:11], off
	s_nop 0
	global_load_dword v12, v[12:13], off
	s_nop 0
	global_load_dword v13, v[22:23], off
	global_load_dword v44, v[42:43], off
	global_load_dword v45, v[46:47], off
	global_load_dword v8, v[58:59], off
	global_load_dword v9, v[60:61], off
	v_add_co_u32_e32 v10, vcc, s42, v4
	s_nop 1
	v_addc_co_u32_e32 v11, vcc, 0, v5, vcc
	v_add_co_u32_e32 v22, vcc, s43, v4
	s_nop 1
	v_addc_co_u32_e32 v23, vcc, 0, v5, vcc
	v_add_co_u32_e32 v42, vcc, s44, v4
	s_nop 1
	v_addc_co_u32_e32 v43, vcc, 0, v5, vcc
	v_add_co_u32_e32 v58, vcc, s45, v4
	s_nop 1
	v_addc_co_u32_e32 v59, vcc, 0, v5, vcc
	v_add_co_u32_e32 v60, vcc, s46, v4
	s_nop 1
	v_addc_co_u32_e32 v61, vcc, 0, v5, vcc
	v_add_co_u32_e32 v62, vcc, 0x74000, v4
	s_nop 1
	v_addc_co_u32_e32 v63, vcc, 0, v5, vcc
	v_add_co_u32_e32 v64, vcc, 0x78000, v4
	s_nop 1
	v_addc_co_u32_e32 v65, vcc, 0, v5, vcc
	v_add_co_u32_e32 v66, vcc, 0x7c000, v4
	s_nop 1
	v_addc_co_u32_e32 v67, vcc, 0, v5, vcc
	global_load_dword v46, v[10:11], off
	global_load_dword v47, v[22:23], off
	s_nop 0
	global_load_dword v10, v[42:43], off
	global_load_dword v11, v[58:59], off
	s_nop 0
	global_load_dword v42, v[60:61], off
	global_load_dword v43, v[62:63], off
	global_load_dword v4, v[64:65], off
	global_load_dword v5, v[66:67], off
	s_and_b64 vcc, exec, s[4:5]
	s_and_b64 vcc, exec, s[4:5]
	s_cbranch_vccnz .Lq_skip_a
	global_load_dword v100, v[6:7], off
	global_load_dword v101, v[6:7], off offset:8
	global_load_dword v102, v[6:7], off offset:16
	global_load_dword v103, v[6:7], off offset:24
	global_load_dword v104, v[6:7], off offset:32
	global_load_dword v105, v[6:7], off offset:40
	global_load_dword v106, v[6:7], off offset:48
	global_load_dword v107, v[6:7], off offset:56
	global_load_dword v108, v[6:7], off offset:64
	global_load_dword v109, v[6:7], off offset:72
	global_load_dword v110, v[6:7], off offset:80
	global_load_dword v111, v[6:7], off offset:88
	global_load_dword v112, v[6:7], off offset:96
	global_load_dword v113, v[6:7], off offset:104
	global_load_dword v114, v[6:7], off offset:112
	global_load_dword v115, v[6:7], off offset:120
	global_load_dword v116, v[6:7], off offset:128
	global_load_dword v117, v[6:7], off offset:136
	global_load_dword v118, v[6:7], off offset:144
	global_load_dword v119, v[6:7], off offset:152
	global_load_dword v120, v[6:7], off offset:160
	global_load_dword v121, v[6:7], off offset:168
	global_load_dword v122, v[6:7], off offset:176
	global_load_dword v123, v[6:7], off offset:184
	global_load_dword v124, v[6:7], off offset:192
	global_load_dword v125, v[6:7], off offset:200
	global_load_dword v126, v[6:7], off offset:208
	global_load_dword v127, v[6:7], off offset:216
	global_load_dword v128, v[6:7], off offset:224
	global_load_dword v129, v[6:7], off offset:232
	global_load_dword v130, v[6:7], off offset:240
	global_load_dword v131, v[6:7], off offset:248
	s_waitcnt vmcnt(0)
.Lq_skip_a:
	s_cbranch_vccnz .LBB0_682
	v_mov_b32_e32 v58, v100
	v_mov_b32_e32 v59, v101
	v_mov_b32_e32 v22, v102
	v_mov_b32_e32 v23, v103
	v_add_u32_e32 v60, v38, v39
	s_waitcnt vmcnt(3)
	v_mul_f32_e32 v58, v56, v58
	s_waitcnt vmcnt(2)
	v_mul_f32_e32 v59, v57, v59
	ds_write2_b32 v60, v58, v59 offset1:66
	s_waitcnt vmcnt(0)
	v_pk_mul_f32 v[22:23], v[20:21], v[22:23]
	s_cbranch_execnz .LBB0_653

.LBB0_653:
	s_and_b64 vcc, exec, s[4:5]
	ds_write2_b32 v30, v22, v23 offset1:66
	s_cbranch_vccnz .LBB0_683
	v_mov_b32_e32 v22, v104
	v_mov_b32_e32 v23, v105
	v_mov_b32_e32 v20, v106
	v_mov_b32_e32 v21, v107
	s_waitcnt vmcnt(35)
	v_add_u32_e32 v56, v38, v40
	s_waitcnt vmcnt(3)
	v_mul_f32_e32 v22, v54, v22
	s_waitcnt vmcnt(2)
	v_mul_f32_e32 v23, v55, v23
	ds_write2_b32 v56, v22, v23 offset1:66
	s_waitcnt vmcnt(0)
	v_pk_mul_f32 v[20:21], v[18:19], v[20:21]
	s_cbranch_execnz .LBB0_656

.LBB0_656:
	s_and_b64 vcc, exec, s[4:5]
	s_waitcnt vmcnt(28)
	ds_write2_b32 v31, v20, v21 offset1:66
	s_cbranch_vccnz .LBB0_684
	v_mov_b32_e32 v20, v108
	v_mov_b32_e32 v21, v109
	v_mov_b32_e32 v18, v110
	v_mov_b32_e32 v19, v111
	v_add_u32_e32 v22, v38, v41
	s_waitcnt vmcnt(3)
	v_mul_f32_e32 v20, v52, v20
	s_waitcnt vmcnt(2)
	v_mul_f32_e32 v21, v53, v21
	ds_write2_b32 v22, v20, v21 offset1:66
	s_waitcnt vmcnt(0)
	v_pk_mul_f32 v[18:19], v[16:17], v[18:19]
	s_cbranch_execnz .LBB0_659

.LBB0_659:
	s_and_b64 vcc, exec, s[4:5]
	s_waitcnt vmcnt(24)
	ds_write2_b32 v32, v18, v19 offset1:66
	s_cbranch_vccnz .LBB0_685
	v_mov_b32_e32 v18, v112
	v_mov_b32_e32 v19, v113
	v_mov_b32_e32 v16, v114
	v_mov_b32_e32 v17, v115
	s_waitcnt vmcnt(3)
	v_mul_f32_e32 v18, v50, v18
	s_waitcnt vmcnt(2)
	v_mul_f32_e32 v19, v51, v19
	ds_write2_b32 v33, v18, v19 offset1:66
	s_waitcnt vmcnt(0)
	v_pk_mul_f32 v[16:17], v[14:15], v[16:17]
	s_cbranch_execnz .LBB0_662

.LBB0_662:
	s_and_b64 vcc, exec, s[4:5]
	s_waitcnt vmcnt(20)
	ds_write2_b32 v34, v16, v17 offset1:66
	s_cbranch_vccnz .LBB0_686
	v_mov_b32_e32 v16, v116
	v_mov_b32_e32 v17, v117
	v_mov_b32_e32 v14, v118
	v_mov_b32_e32 v15, v119
	s_waitcnt vmcnt(3)
	v_mul_f32_e32 v16, v48, v16
	s_waitcnt vmcnt(2)
	v_mul_f32_e32 v17, v49, v17
	ds_write2_b32 v35, v16, v17 offset1:66
	s_waitcnt vmcnt(0)
	v_pk_mul_f32 v[14:15], v[12:13], v[14:15]
	s_cbranch_execnz .LBB0_665

.LBB0_665:
	s_and_b64 vcc, exec, s[4:5]
	s_waitcnt vmcnt(16)
	ds_write2_b32 v36, v14, v15 offset1:66
	s_cbranch_vccnz .LBB0_687
	v_mov_b32_e32 v14, v120
	v_mov_b32_e32 v15, v121
	v_mov_b32_e32 v12, v122
	v_mov_b32_e32 v13, v123
	s_waitcnt vmcnt(3)
	v_mul_f32_e32 v14, v44, v14
	s_waitcnt vmcnt(2)
	v_mul_f32_e32 v15, v45, v15
	ds_write2_b32 v37, v14, v15 offset1:66
	s_waitcnt vmcnt(0)
	v_pk_mul_f32 v[12:13], v[8:9], v[12:13]
	s_cbranch_execnz .LBB0_668

.LBB0_668:
	s_waitcnt vmcnt(12)
	ds_write2_b32 v37, v12, v13 offset0:132 offset1:198
	s_and_b64 vcc, exec, s[4:5]
	v_add_u32_e32 v12, 0x400, v37
	s_cbranch_vccnz .LBB0_688
	v_mov_b32_e32 v13, v124
	v_mov_b32_e32 v14, v125
	v_mov_b32_e32 v8, v126
	v_mov_b32_e32 v9, v127
	s_waitcnt vmcnt(3)
	v_mul_f32_e32 v13, v46, v13
	s_waitcnt vmcnt(2)
	v_mul_f32_e32 v14, v47, v14
	ds_write2_b32 v12, v13, v14 offset0:8 offset1:74
	s_waitcnt vmcnt(0)
	v_pk_mul_f32 v[8:9], v[10:11], v[8:9]
	s_cbranch_execnz .LBB0_671

.LBB0_671:
	s_waitcnt vmcnt(8)
	ds_write2_b32 v12, v8, v9 offset0:140 offset1:206
	s_and_b64 vcc, exec, s[4:5]
	v_add_u32_e32 v8, 0x800, v37
	s_cbranch_vccnz .LBB0_689
	v_mov_b32_e32 v9, v128
	v_mov_b32_e32 v12, v129
	v_mov_b32_e32 v10, v130
	v_mov_b32_e32 v11, v131
	s_waitcnt vmcnt(3)
	v_mul_f32_e32 v9, v42, v9
	s_waitcnt vmcnt(2)
	v_mul_f32_e32 v12, v43, v12
	ds_write2_b32 v8, v9, v12 offset0:16 offset1:82
	s_waitcnt vmcnt(0)
	v_pk_mul_f32 v[6:7], v[4:5], v[10:11]
	s_cbranch_execnz .LBB0_674

.LBB0_692:
	s_ashr_i32 s22, s19, 11
	v_readlane_b32 s72, v251, 2
	s_mul_i32 s7, s22, 0x1800000
	v_readlane_b32 s78, v251, 8
	s_mul_hi_i32 s6, s22, 0x1800000
	v_readlane_b32 s79, v251, 9
	s_add_u32 s23, s78, s7
	s_addc_u32 s25, s79, s6
	s_and_b32 s6, s19, 0xfffff800
	s_ashr_i32 s7, s6, 31
	v_readlane_b32 s76, v251, 6
	s_lshl_b64 s[6:7], s[6:7], 2
	v_readlane_b32 s77, v251, 7
	s_add_u32 s8, s76, s6
	s_addc_u32 s9, s77, s7
	s_lshl_b32 s20, s19, 5
	s_and_b32 s20, s20, 0x7e0
	s_and_b32 s21, s19, 0x7c0
	s_lshl_b32 s24, s20, 2
	s_add_u32 s24, s23, s24
	v_add_u32_e32 v6, s21, v24
	s_addc_u32 s25, s25, 0
	v_lshl_add_u64 v[4:5], s[24:25], 0, v[2:3]
	v_add_u32_e32 v7, 2, v6
	v_mad_i64_i32 v[10:11], s[24:25], v7, s16, v[4:5]
	v_add_u32_e32 v7, 4, v6
	v_mad_i64_i32 v[12:13], s[24:25], v7, s16, v[4:5]
	v_add_u32_e32 v7, 6, v6
	v_mad_i64_i32 v[14:15], s[24:25], v7, s16, v[4:5]
	v_add_u32_e32 v7, 8, v6
	v_mad_i64_i32 v[16:17], s[24:25], v7, s16, v[4:5]
	v_add_u32_e32 v7, 10, v6
	v_mad_i64_i32 v[18:19], s[24:25], v7, s16, v[4:5]
	v_add_u32_e32 v7, 12, v6
	v_mad_i64_i32 v[22:23], s[24:25], v7, s16, v[4:5]
	v_add_u32_e32 v7, 14, v6
	v_mad_i64_i32 v[8:9], s[24:25], v6, s16, v[4:5]
	v_mad_i64_i32 v[42:43], s[24:25], v7, s16, v[4:5]
	v_add_u32_e32 v7, 16, v6
	global_load_dword v55, v[8:9], off
	global_load_dword v56, v[10:11], off
	global_load_dword v20, v[12:13], off
	global_load_dword v21, v[14:15], off
	global_load_dword v53, v[16:17], off
	global_load_dword v54, v[18:19], off
	s_nop 0
	global_load_dword v18, v[22:23], off
	global_load_dword v19, v[42:43], off
	v_mad_i64_i32 v[8:9], s[24:25], v7, s16, v[4:5]
	v_add_u32_e32 v7, 18, v6
	v_mad_i64_i32 v[10:11], s[24:25], v7, s16, v[4:5]
	v_add_u32_e32 v7, 20, v6
	v_mad_i64_i32 v[12:13], s[24:25], v7, s16, v[4:5]
	v_add_u32_e32 v7, 22, v6
	v_mad_i64_i32 v[14:15], s[24:25], v7, s16, v[4:5]
	v_add_u32_e32 v7, 24, v6
	v_mad_i64_i32 v[22:23], s[24:25], v7, s16, v[4:5]
	v_add_u32_e32 v7, 26, v6
	v_mad_i64_i32 v[42:43], s[24:25], v7, s16, v[4:5]
	v_add_u32_e32 v7, 28, v6
	v_mad_i64_i32 v[44:45], s[24:25], v7, s16, v[4:5]
	v_add_u32_e32 v7, 30, v6
	v_mad_i64_i32 v[46:47], s[24:25], v7, s16, v[4:5]
	v_add_u32_e32 v7, 32, v6
	global_load_dword v51, v[8:9], off
	global_load_dword v52, v[10:11], off
	global_load_dword v16, v[12:13], off
	global_load_dword v17, v[14:15], off
	global_load_dword v49, v[22:23], off
	global_load_dword v50, v[42:43], off
	s_nop 0
	global_load_dword v14, v[44:45], off
	global_load_dword v15, v[46:47], off
	v_mad_i64_i32 v[8:9], s[24:25], v7, s16, v[4:5]
	v_add_u32_e32 v7, 34, v6
	v_mad_i64_i32 v[10:11], s[24:25], v7, s16, v[4:5]
	v_add_u32_e32 v7, 36, v6
	v_mad_i64_i32 v[12:13], s[24:25], v7, s16, v[4:5]
	v_add_u32_e32 v7, 38, v6
	v_mad_i64_i32 v[22:23], s[24:25], v7, s16, v[4:5]
	v_add_u32_e32 v7, 40, v6
	v_mad_i64_i32 v[42:43], s[24:25], v7, s16, v[4:5]
	v_add_u32_e32 v7, 42, v6
	v_mad_i64_i32 v[58:59], s[24:25], v7, s16, v[4:5]
	v_add_u32_e32 v7, 44, v6
	v_mad_i64_i32 v[60:61], s[24:25], v7, s16, v[4:5]
	v_add_u32_e32 v7, 46, v6
	v_mad_i64_i32 v[62:63], s[24:25], v7, s16, v[4:5]
	v_add_u32_e32 v7, 48, v6
	global_load_dword v47, v[8:9], off
	global_load_dword v48, v[10:11], off
	s_nop 0
	global_load_dword v12, v[12:13], off
	s_nop 0
	global_load_dword v13, v[22:23], off
	global_load_dword v45, v[42:43], off
	global_load_dword v46, v[58:59], off
	global_load_dword v10, v[60:61], off
	global_load_dword v11, v[62:63], off
	v_mad_i64_i32 v[8:9], s[24:25], v7, s16, v[4:5]
	v_add_u32_e32 v7, 50, v6
	v_mad_i64_i32 v[22:23], s[24:25], v7, s16, v[4:5]
	v_add_u32_e32 v7, 52, v6
	v_mad_i64_i32 v[58:59], s[24:25], v7, s16, v[4:5]
	v_add_u32_e32 v7, 54, v6
	v_mad_i64_i32 v[60:61], s[24:25], v7, s16, v[4:5]
	v_add_u32_e32 v7, 56, v6
	v_mad_i64_i32 v[62:63], s[24:25], v7, s16, v[4:5]
	v_add_u32_e32 v7, 58, v6
	v_mad_i64_i32 v[64:65], s[24:25], v7, s16, v[4:5]
	v_add_u32_e32 v7, 60, v6
	v_mad_i64_i32 v[66:67], s[24:25], v7, s16, v[4:5]
	v_add_u32_e32 v7, 62, v6
	v_mad_i64_i32 v[68:69], s[24:25], v7, s16, v[4:5]
	global_load_dword v43, v[8:9], off
	global_load_dword v44, v[22:23], off
	s_nop 0
	global_load_dword v8, v[58:59], off
	global_load_dword v9, v[60:61], off
	global_load_dword v41, v[62:63], off
	global_load_dword v42, v[64:65], off
	global_load_dword v4, v[66:67], off
	global_load_dword v5, v[68:69], off
	v_ashrrev_i32_e32 v7, 31, v6
	s_and_b64 vcc, exec, s[4:5]
	v_lshl_add_u64 v[6:7], v[6:7], 2, s[8:9]
	v_readlane_b32 s73, v251, 3
	v_readlane_b32 s74, v251, 4
	v_readlane_b32 s75, v251, 5
	v_readlane_b32 s80, v251, 10
	v_readlane_b32 s81, v251, 11
	v_readlane_b32 s82, v251, 12
	v_readlane_b32 s83, v251, 13
	v_readlane_b32 s84, v251, 14
	v_readlane_b32 s85, v251, 15
	v_readlane_b32 s86, v251, 16
	v_readlane_b32 s87, v251, 17
	s_and_b64 vcc, exec, s[4:5]
	s_cbranch_vccnz .Lq_skip_b
	global_load_dword v100, v[6:7], off
	global_load_dword v101, v[6:7], off offset:8
	global_load_dword v102, v[6:7], off offset:16
	global_load_dword v103, v[6:7], off offset:24
	global_load_dword v104, v[6:7], off offset:32
	global_load_dword v105, v[6:7], off offset:40
	global_load_dword v106, v[6:7], off offset:48
	global_load_dword v107, v[6:7], off offset:56
	global_load_dword v108, v[6:7], off offset:64
	global_load_dword v109, v[6:7], off offset:72
	global_load_dword v110, v[6:7], off offset:80
	global_load_dword v111, v[6:7], off offset:88
	global_load_dword v112, v[6:7], off offset:96
	global_load_dword v113, v[6:7], off offset:104
	global_load_dword v114, v[6:7], off offset:112
	global_load_dword v115, v[6:7], off offset:120
	global_load_dword v116, v[6:7], off offset:128
	global_load_dword v117, v[6:7], off offset:136
	global_load_dword v118, v[6:7], off offset:144
	global_load_dword v119, v[6:7], off offset:152
	global_load_dword v120, v[6:7], off offset:160
	global_load_dword v121, v[6:7], off offset:168
	global_load_dword v122, v[6:7], off offset:176
	global_load_dword v123, v[6:7], off offset:184
	global_load_dword v124, v[6:7], off offset:192
	global_load_dword v125, v[6:7], off offset:200
	global_load_dword v126, v[6:7], off offset:208
	global_load_dword v127, v[6:7], off offset:216
	global_load_dword v128, v[6:7], off offset:224
	global_load_dword v129, v[6:7], off offset:232
	global_load_dword v130, v[6:7], off offset:240
	global_load_dword v131, v[6:7], off offset:248
	s_waitcnt vmcnt(0)
.Lq_skip_b:
	s_cbranch_vccnz .LBB0_694
	v_mov_b32_e32 v57, v100
	v_mov_b32_e32 v58, v101
	v_mov_b32_e32 v22, v102
	v_mov_b32_e32 v23, v103
	s_mov_b64 s[8:9], 0
	s_waitcnt vmcnt(3)
	v_mul_f32_e32 v57, v55, v57
	s_waitcnt vmcnt(2)
	v_mul_f32_e32 v58, v56, v58
	ds_write2_b32 v39, v57, v58 offset1:66
	s_waitcnt vmcnt(0)
	v_pk_mul_f32 v[22:23], v[20:21], v[22:23]
	s_branch .LBB0_695

.LBB0_697:
	v_readlane_b32 s78, v251, 36
	s_and_b64 vcc, exec, s[4:5]
	v_readlane_b32 s79, v251, 37
	ds_write2_b32 v30, v22, v23 offset1:66
	s_cbranch_vccnz .LBB0_726
	v_mov_b32_e32 v22, v104
	v_mov_b32_e32 v23, v105
	v_mov_b32_e32 v20, v106
	v_mov_b32_e32 v21, v107
	s_waitcnt vmcnt(3)
	v_mul_f32_e32 v22, v53, v22
	s_waitcnt vmcnt(2)
	v_mul_f32_e32 v23, v54, v23
	ds_write2_b32 v40, v22, v23 offset1:66
	s_waitcnt vmcnt(0)
	v_pk_mul_f32 v[20:21], v[18:19], v[20:21]
	s_cbranch_execnz .LBB0_700

.LBB0_700:
	s_and_b64 vcc, exec, s[4:5]
	s_waitcnt vmcnt(28)
	ds_write2_b32 v31, v20, v21 offset1:66
	s_cbranch_vccnz .LBB0_727
	v_mov_b32_e32 v20, v108
	v_mov_b32_e32 v21, v109
	v_mov_b32_e32 v18, v110
	v_mov_b32_e32 v19, v111
	s_waitcnt vmcnt(3)
	v_mul_f32_e32 v20, v51, v20
	s_waitcnt vmcnt(2)
	v_mul_f32_e32 v21, v52, v21
	ds_write2_b32 v38, v20, v21 offset1:66
	s_waitcnt vmcnt(0)
	v_pk_mul_f32 v[18:19], v[16:17], v[18:19]
	s_cbranch_execnz .LBB0_703

.LBB0_703:
	s_and_b64 vcc, exec, s[4:5]
	s_waitcnt vmcnt(24)
	ds_write2_b32 v32, v18, v19 offset1:66
	s_cbranch_vccnz .LBB0_728
	v_mov_b32_e32 v18, v112
	v_mov_b32_e32 v19, v113
	v_mov_b32_e32 v16, v114
	v_mov_b32_e32 v17, v115
	s_waitcnt vmcnt(3)
	v_mul_f32_e32 v18, v49, v18
	s_waitcnt vmcnt(2)
	v_mul_f32_e32 v19, v50, v19
	ds_write2_b32 v33, v18, v19 offset1:66
	s_waitcnt vmcnt(0)
	v_pk_mul_f32 v[16:17], v[14:15], v[16:17]
	s_cbranch_execnz .LBB0_706

.LBB0_706:
	s_and_b64 vcc, exec, s[4:5]
	s_waitcnt vmcnt(20)
	ds_write2_b32 v34, v16, v17 offset1:66
	s_cbranch_vccnz .LBB0_729
	v_mov_b32_e32 v16, v116
	v_mov_b32_e32 v17, v117
	v_mov_b32_e32 v14, v118
	v_mov_b32_e32 v15, v119
	s_waitcnt vmcnt(3)
	v_mul_f32_e32 v16, v47, v16
	s_waitcnt vmcnt(2)
	v_mul_f32_e32 v17, v48, v17
	ds_write2_b32 v35, v16, v17 offset1:66
	s_waitcnt vmcnt(0)
	v_pk_mul_f32 v[14:15], v[12:13], v[14:15]
	s_cbranch_execnz .LBB0_709

.LBB0_709:
	s_and_b64 vcc, exec, s[4:5]
	s_waitcnt vmcnt(16)
	ds_write2_b32 v36, v14, v15 offset1:66
	s_cbranch_vccnz .LBB0_730
	v_mov_b32_e32 v14, v120
	v_mov_b32_e32 v15, v121
	v_mov_b32_e32 v12, v122
	v_mov_b32_e32 v13, v123
	s_waitcnt vmcnt(3)
	v_mul_f32_e32 v14, v45, v14
	s_waitcnt vmcnt(2)
	v_mul_f32_e32 v15, v46, v15
	ds_write2_b32 v37, v14, v15 offset1:66
	s_waitcnt vmcnt(0)
	v_pk_mul_f32 v[12:13], v[10:11], v[12:13]
	s_cbranch_execnz .LBB0_712

.LBB0_712:
	s_waitcnt vmcnt(12)
	ds_write2_b32 v37, v12, v13 offset0:132 offset1:198
	s_and_b64 vcc, exec, s[4:5]
	v_add_u32_e32 v12, 0x400, v37
	s_cbranch_vccnz .LBB0_731
	v_mov_b32_e32 v13, v124
	v_mov_b32_e32 v14, v125
	v_mov_b32_e32 v10, v126
	v_mov_b32_e32 v11, v127
	s_waitcnt vmcnt(3)
	v_mul_f32_e32 v13, v43, v13
	s_waitcnt vmcnt(2)
	v_mul_f32_e32 v14, v44, v14
	ds_write2_b32 v12, v13, v14 offset0:8 offset1:74
	s_waitcnt vmcnt(0)
	v_pk_mul_f32 v[10:11], v[8:9], v[10:11]
	s_cbranch_execnz .LBB0_715

.LBB0_715:
	s_and_b64 vcc, exec, s[4:5]
	s_waitcnt vmcnt(5)
	v_add_u32_e32 v8, 0x800, v37
	ds_write2_b32 v12, v10, v11 offset0:140 offset1:206
	s_cbranch_vccnz .LBB0_732
	v_mov_b32_e32 v9, v128
	v_mov_b32_e32 v12, v129
	v_mov_b32_e32 v10, v130
	v_mov_b32_e32 v11, v131
	s_waitcnt vmcnt(3)
	v_mul_f32_e32 v9, v41, v9
	s_waitcnt vmcnt(2)
	v_mul_f32_e32 v12, v42, v12
	ds_write2_b32 v8, v9, v12 offset0:16 offset1:82
	s_waitcnt vmcnt(0)
	v_pk_mul_f32 v[6:7], v[4:5], v[10:11]
	s_cbranch_execnz .LBB0_718

.LBB0_919:
	v_readlane_b32 s54, v251, 58
	s_andn2_b64 vcc, exec, s[2:3]
	v_readlane_b32 s55, v251, 59
	s_cbranch_vccnz .LBB0_1001
	v_readlane_b32 s0, v251, 60
	s_waitcnt lgkmcnt(0)
	v_mbcnt_lo_u32_b32 v7, -1, 0
	v_mbcnt_hi_u32_b32 v7, -1, v7
	v_readlane_b32 s1, v251, 61
	v_add_u32_e32 v0, s63, v7
	s_andn2_b64 vcc, exec, s[0:1]
	v_readfirstlane_b32 s6, v0
	s_cbranch_vccnz .LBB0_945
	v_lshlrev_b32_e32 v1, 4, v0
	v_add_u32_e32 v2, 0x2000, v1
	v_ashrrev_i32_e32 v3, 31, v2
	v_lshrrev_b32_e32 v3, 22, v3
	v_add_u32_e32 v3, v2, v3
	v_ashrrev_i32_e32 v4, 10, v3
	v_mul_i32_i24_e32 v3, 0x400, v4
	v_sub_u32_e32 v2, v2, v3
	v_lshrrev_b32_e32 v3, 4, v2
	v_bitop3_b32 v2, v3, v2, 32 bitop3:0x6c
	v_ashrrev_i32_e32 v3, 31, v2
	v_lshrrev_b32_e32 v3, 26, v3
	v_add_u32_e32 v3, v2, v3
	v_lshlrev_b32_e32 v6, 3, v4
	s_mul_i32 s2, s38, 0x600000
	v_readlane_b32 s0, v252, 6
	v_ashrrev_i32_e32 v5, 6, v3
	v_and_b32_e32 v6, -16, v6
	s_add_u32 s26, s0, s2
	v_readlane_b32 s0, v252, 7
	v_add_u32_e32 v8, v5, v6
	s_addc_u32 s27, s0, 0
	v_and_b32_e32 v6, 3, v5
	s_mov_b32 s0, 0x1fffe0
	v_lshrrev_b32_e32 v9, 2, v8
	s_waitcnt vmcnt(0)
	v_lshlrev_b32_e32 v10, 1, v8
	v_and_b32_e32 v3, 0xc0, v3
	v_and_or_b32 v6, v8, s0, v6
	v_and_b32_e32 v9, 4, v9
	v_and_b32_e32 v10, 24, v10
	v_sub_u32_e32 v2, v2, v3
	v_or3_b32 v9, v6, v9, v10
	v_lshlrev_b32_e32 v6, 5, v4
	v_ashrrev_i16_sdwa v2, v227, sext(v2) dst_sel:DWORD dst_unused:UNUSED_PAD src0_sel:DWORD src1_sel:BYTE_0
	v_and_b32_e32 v10, 32, v6
	v_bfe_i32 v6, v2, 0, 16
	v_add_lshl_u32 v2, v10, v6, 1
	v_lshl_add_u32 v144, v9, 11, v2
	v_lshl_add_u32 v146, v8, 11, v2
	v_bfe_i32 v2, v0, 27, 1
	v_lshrrev_b32_e32 v2, 22, v2
	v_add_u32_e32 v2, v1, v2
	v_and_b32_e32 v2, 0xfffffc00, v2
	v_sub_u32_e32 v1, v1, v2
	v_lshrrev_b32_e32 v2, 4, v1
	v_ashrrev_i32_e32 v3, 31, v0
	v_bitop3_b32 v1, v2, v1, 32 bitop3:0x6c
	v_lshrrev_b32_e32 v3, 26, v3
	v_ashrrev_i32_e32 v2, 31, v1
	v_add_u32_e32 v0, v0, v3
	v_lshrrev_b32_e32 v2, 26, v2
	v_ashrrev_i32_e32 v9, 6, v0
	v_add_u32_e32 v2, v1, v2
	v_lshlrev_b32_e32 v0, 3, v9
	v_ashrrev_i32_e32 v8, 6, v2
	v_and_b32_e32 v0, -16, v0
	v_add_u32_e32 v0, v8, v0
	v_and_b32_e32 v3, 3, v8
	v_lshrrev_b32_e32 v10, 2, v0
	v_lshlrev_b32_e32 v11, 1, v0
	v_and_b32_e32 v2, 0xc0, v2
	s_ashr_i32 s7, s6, 6
	v_and_or_b32 v3, v0, s0, v3
	v_and_b32_e32 v10, 4, v10
	v_and_b32_e32 v11, 24, v11
	v_sub_u32_e32 v1, v1, v2
	s_lshl_b32 s28, s7, 10
	v_or3_b32 v3, v3, v10, v11
	v_lshlrev_b32_e32 v10, 5, v9
	v_ashrrev_i16_sdwa v1, v227, sext(v1) dst_sel:DWORD dst_unused:UNUSED_PAD src0_sel:DWORD src1_sel:BYTE_0
	v_readlane_b32 s0, v252, 15
	v_and_b32_e32 v11, 32, v10
	v_bfe_i32 v10, v1, 0, 16
	v_readlane_b32 s1, v252, 16
	s_add_u32 s20, s26, s0
	v_add_lshl_u32 v1, v11, v10, 1
	s_addc_u32 s21, s27, s1
	s_add_i32 s29, s28, 0
	v_lshl_add_u32 v200, v3, 11, v1
	s_add_i32 m0, s29, 0x10000
	v_readlane_b32 s0, v254, 42
	global_load_lds_dwordx4 v200, s[20:21]
	s_add_i32 m0, s29, 0x12000
	s_add_u32 s2, s20, 0x40000
	global_load_lds_dwordx4 v144, s[20:21]
	s_addc_u32 s3, s21, 0
	s_add_i32 m0, s29, 0x14000
	v_lshl_add_u32 v148, v0, 11, v1
	global_load_lds_dwordx4 v200, s[2:3]
	s_add_i32 m0, s29, 0x16000
	v_readlane_b32 s1, v254, 43
	global_load_lds_dwordx4 v144, s[2:3]
	s_mov_b32 m0, s29
	s_add_i32 s30, s29, 0x2000
	s_add_i32 s31, s29, 0x4000
	s_nop 0
	global_load_lds_dwordx4 v148, s[0:1]
	s_mov_b32 m0, s30
	s_add_i32 s34, s29, 0x6000
	global_load_lds_dwordx4 v146, s[0:1]
	v_readlane_b32 s0, v254, 44
	s_mov_b32 m0, s31
	v_readlane_b32 s1, v254, 45
	v_mov_b32_e32 v15, v201
	s_nop 3
	global_load_lds_dwordx4 v148, s[0:1]
	s_mov_b32 m0, s34
	s_nop 0
	global_load_lds_dwordx4 v146, s[0:1]
	v_mbcnt_lo_u32_b32 v0, -1, 0
	v_mbcnt_hi_u32_b32 v0, -1, v0
	v_readlane_b32 s0, v252, 17
	v_readlane_b32 s1, v252, 18
	v_readlane_b32 s10, v252, 19
	v_readlane_b32 s11, v252, 20
	v_add_u32_e32 v0, s63, v0
	v_ashrrev_i32_e32 v2, 1, v0
	v_and_b32_e32 v22, 1, v0
	v_lshlrev_b32_e32 v14, 6, v22
	v_mov_b32_e32 v15, v201
	s_mov_b32 s9, 1
	v_readlane_b32 s14, v252, 21
	s_nop 1
	v_add_u32_e32 v40, s14, v2
	v_ashrrev_i32_e32 v41, 31, v40
	v_lshlrev_b64 v[12:13], 7, v[40:41]
	v_lshl_add_u64 v[12:13], s[0:1], 0, v[12:13]
	v_lshl_add_u64 v[20:21], v[12:13], 0, v[14:15]
	global_load_dwordx4 v[24:27], v[20:21], off offset:16
	global_load_dwordx4 v[28:31], v[20:21], off
	global_load_dwordx4 v[32:35], v[20:21], off offset:48
	global_load_dwordx4 v[36:39], v[20:21], off offset:32
	v_lshl_add_u64 v[40:41], v[40:41], 2, s[10:11]
	global_load_dword v42, v[40:41], off
	v_readlane_b32 s12, v252, 22
	v_readlane_b32 s13, v252, 23
	s_andn2_b64 vcc, exec, s[12:13]
	s_cbranch_vccnz .Lpre1_loaded
	s_mov_b32 s9, 2
	v_readlane_b32 s14, v254, 46
	s_nop 1
	v_add_u32_e32 v60, s14, v2
	v_ashrrev_i32_e32 v61, 31, v60
	v_lshlrev_b64 v[12:13], 7, v[60:61]
	v_lshl_add_u64 v[12:13], s[0:1], 0, v[12:13]
	v_lshl_add_u64 v[20:21], v[12:13], 0, v[14:15]
	global_load_dwordx4 v[44:47], v[20:21], off offset:16
	global_load_dwordx4 v[48:51], v[20:21], off
	global_load_dwordx4 v[52:55], v[20:21], off offset:48
	global_load_dwordx4 v[56:59], v[20:21], off offset:32
	v_lshl_add_u64 v[60:61], v[60:61], 2, s[10:11]
	global_load_dword v62, v[60:61], off
	v_readlane_b32 s12, v252, 24
	v_readlane_b32 s13, v252, 25
	s_andn2_b64 vcc, exec, s[12:13]
	s_cbranch_vccnz .Lpre1_loaded
	s_mov_b32 s9, 3
	v_readlane_b32 s14, v254, 47
	s_nop 1
	v_add_u32_e32 v80, s14, v2
	v_ashrrev_i32_e32 v81, 31, v80
	v_lshlrev_b64 v[12:13], 7, v[80:81]
	v_lshl_add_u64 v[12:13], s[0:1], 0, v[12:13]
	v_lshl_add_u64 v[20:21], v[12:13], 0, v[14:15]
	global_load_dwordx4 v[64:67], v[20:21], off offset:16
	global_load_dwordx4 v[68:71], v[20:21], off
	global_load_dwordx4 v[72:75], v[20:21], off offset:48
	global_load_dwordx4 v[76:79], v[20:21], off offset:32
	v_lshl_add_u64 v[80:81], v[80:81], 2, s[10:11]
	global_load_dword v82, v[80:81], off
.Lpre1_loaded:
	v_cmp_eq_u32_e32 vcc, 0, v22
	s_mov_b64 s[12:13], vcc
	v_lshl_add_u32 v2, v2, 2, 0
	s_waitcnt vmcnt(0)
	v_add_f32_e32 v3, v28, v29
	v_add_f32_e32 v11, v30, v31
	v_add_f32_e32 v3, v3, v11
	v_add_f32_e32 v11, v24, v25
	v_add_f32_e32 v12, v26, v27
	v_add_f32_e32 v11, v11, v12
	v_add_f32_e32 v3, v3, v11
	v_add_f32_e32 v12, v32, v33
	v_add_f32_e32 v11, v36, v37
	v_add_f32_e32 v16, v38, v39
	v_add_f32_e32 v13, v34, v35
	v_add_f32_e32 v11, v11, v16
	v_add_f32_e32 v12, v12, v13
	v_add_f32_e32 v11, v11, v12
	v_add_f32_e32 v3, v3, v11
	v_mov_b32_e32 v11, v201
	s_nop 1
	v_mov_b32_dpp v11, v3 quad_perm:[1,0,3,2] row_mask:0xf bank_mask:0xf
	s_mov_b64 exec, s[12:13]
	v_add_f32_e32 v1, v3, v11
	v_mov_b32_e32 v3, 0x358637bd
	v_fmamk_f32 v1, v1, 0x3a000000, v3
	s_mov_b32 s14, 0x800000
	v_mul_f32_e32 v3, 0x4b800000, v1
	v_cmp_gt_f32_e32 vcc, s14, v1
	s_nop 1
	v_cndmask_b32_e32 v1, v1, v3, vcc
	v_rsq_f32_e32 v1, v1
	s_nop 0
	v_mul_f32_e32 v3, 0x45800000, v1
	v_cndmask_b32_e32 v1, v1, v3, vcc
	v_div_scale_f32 v3, s[4:5], v42, v42, v1
	v_rcp_f32_e32 v11, v3
	v_div_scale_f32 v12, vcc, v1, v42, v1
	v_fma_f32 v13, -v3, v11, 1.0
	v_fmac_f32_e32 v11, v13, v11
	v_mul_f32_e32 v13, v12, v11
	v_fma_f32 v14, -v3, v13, v12
	v_fmac_f32_e32 v13, v14, v11
	v_fma_f32 v3, -v3, v13, v12
	v_div_fmas_f32 v3, v3, v11, v13
	v_div_fixup_f32 v0, v3, v42, v1
	v_add_u32_e32 v1, 0x25000, v2
	ds_write_b32 v1, v0
	s_mov_b64 exec, -1
	s_cmp_lt_u32 s9, 2
	s_cbranch_scc1 .Lpre1_done
	v_add_f32_e32 v3, v48, v49
	v_add_f32_e32 v11, v50, v51
	v_add_f32_e32 v3, v3, v11
	v_add_f32_e32 v11, v44, v45
	v_add_f32_e32 v12, v46, v47
	v_add_f32_e32 v11, v11, v12
	v_add_f32_e32 v3, v3, v11
	v_add_f32_e32 v12, v52, v53
	v_add_f32_e32 v11, v56, v57
	v_add_f32_e32 v16, v58, v59
	v_add_f32_e32 v13, v54, v55
	v_add_f32_e32 v11, v11, v16
	v_add_f32_e32 v12, v12, v13
	v_add_f32_e32 v11, v11, v12
	v_add_f32_e32 v3, v3, v11
	v_mov_b32_e32 v11, v201
	s_nop 1
	v_mov_b32_dpp v11, v3 quad_perm:[1,0,3,2] row_mask:0xf bank_mask:0xf
	s_mov_b64 exec, s[12:13]
	v_add_f32_e32 v1, v3, v11
	v_mov_b32_e32 v3, 0x358637bd
	v_fmamk_f32 v1, v1, 0x3a000000, v3
	s_mov_b32 s14, 0x800000
	v_mul_f32_e32 v3, 0x4b800000, v1
	v_cmp_gt_f32_e32 vcc, s14, v1
	s_nop 1
	v_cndmask_b32_e32 v1, v1, v3, vcc
	v_rsq_f32_e32 v1, v1
	s_nop 0
	v_mul_f32_e32 v3, 0x45800000, v1
	v_cndmask_b32_e32 v1, v1, v3, vcc
	v_div_scale_f32 v3, s[4:5], v62, v62, v1
	v_rcp_f32_e32 v11, v3
	v_div_scale_f32 v12, vcc, v1, v62, v1
	v_fma_f32 v13, -v3, v11, 1.0
	v_fmac_f32_e32 v11, v13, v11
	v_mul_f32_e32 v13, v12, v11
	v_fma_f32 v14, -v3, v13, v12
	v_fmac_f32_e32 v13, v14, v11
	v_fma_f32 v3, -v3, v13, v12
	v_div_fmas_f32 v3, v3, v11, v13
	v_div_fixup_f32 v0, v3, v62, v1
	v_add_u32_e32 v1, 0x25400, v2
	ds_write_b32 v1, v0
	s_mov_b64 exec, -1
	s_cmp_lt_u32 s9, 3
	s_cbranch_scc1 .Lpre1_done
	v_add_f32_e32 v3, v68, v69
	v_add_f32_e32 v11, v70, v71
	v_add_f32_e32 v3, v3, v11
	v_add_f32_e32 v11, v64, v65
	v_add_f32_e32 v12, v66, v67
	v_add_f32_e32 v11, v11, v12
	v_add_f32_e32 v3, v3, v11
	v_add_f32_e32 v12, v72, v73
	v_add_f32_e32 v11, v76, v77
	v_add_f32_e32 v16, v78, v79
	v_add_f32_e32 v13, v74, v75
	v_add_f32_e32 v11, v11, v16
	v_add_f32_e32 v12, v12, v13
	v_add_f32_e32 v11, v11, v12
	v_add_f32_e32 v3, v3, v11
	v_mov_b32_e32 v11, v201
	s_nop 1
	v_mov_b32_dpp v11, v3 quad_perm:[1,0,3,2] row_mask:0xf bank_mask:0xf
	s_mov_b64 exec, s[12:13]
	v_add_f32_e32 v1, v3, v11
	v_mov_b32_e32 v3, 0x358637bd
	v_fmamk_f32 v1, v1, 0x3a000000, v3
	s_mov_b32 s14, 0x800000
	v_mul_f32_e32 v3, 0x4b800000, v1
	v_cmp_gt_f32_e32 vcc, s14, v1
	s_nop 1
	v_cndmask_b32_e32 v1, v1, v3, vcc
	v_rsq_f32_e32 v1, v1
	s_nop 0
	v_mul_f32_e32 v3, 0x45800000, v1
	v_cndmask_b32_e32 v1, v1, v3, vcc
	v_div_scale_f32 v3, s[4:5], v82, v82, v1
	v_rcp_f32_e32 v11, v3
	v_div_scale_f32 v12, vcc, v1, v82, v1
	v_fma_f32 v13, -v3, v11, 1.0
	v_fmac_f32_e32 v11, v13, v11
	v_mul_f32_e32 v13, v12, v11
	v_fma_f32 v14, -v3, v13, v12
	v_fmac_f32_e32 v13, v14, v11
	v_fma_f32 v3, -v3, v13, v12
	v_div_fmas_f32 v3, v3, v11, v13
	v_div_fixup_f32 v0, v3, v82, v1
	v_add_u32_e32 v1, 0x25800, v2
	ds_write_b32 v1, v0
	s_mov_b64 exec, -1
.Lpre1_done:
	s_mov_b64 exec, -1
